# redundant wait-state pads after the fp8 K-loops of P5 and P16 removed
# baseline (speedup 1.0000x reference)
; #define PG8_STAGE(bufoff, gbase, o0, o1) do { \
;         __builtin_amdgcn_global_load_lds((const unsigned*)((const char*)(gbase) + (o0)), (LAS unsigned*)(lds + (bufoff) + ldsw), 16, 0, 0); \
;         __builtin_amdgcn_global_load_lds((const unsigned*)((const char*)(gbase) + (o1)), (LAS unsigned*)(lds + (bufoff) + ldsw + 8192), 16, 0, 0); } while (0)
; #define PG8_LDA(dst, b, h) do { _Pragma("unroll") for (int m = 0; m < 4; ++m) _Pragma("unroll") for (int k = 0; k < 2; ++k) dst[m][k] = *(const LAS bf16x8*)(lds + PG8_SA(b, h) + aoff + m * 2048 + k * 1024); } while (0)
; #define PG8_LDB(dst, b, h) do { _Pragma("unroll") for (int n = 0; n < 2; ++n) _Pragma("unroll") for (int k = 0; k < 2; ++k) dst[n][k] = *(const LAS bf16x8*)(lds + PG8_SB(b, h) + boff + n * 2048 + k * 1024); } while (0)
; #define PG8_WAIT_V(n) asm volatile("s_waitcnt vmcnt(" #n ")" ::: "memory")
; #define PG8_WAIT_L(n) asm volatile("s_waitcnt lgkmcnt(" #n ")" ::: "memory")
; #define PG8_BAR __builtin_amdgcn_s_barrier()
; #define PG8_SCHED __builtin_amdgcn_sched_barrier(0)
; template <class Epi, class Sched, class Prob>
; __device__ __forceinline__ void gemm_phase(LAS unsigned char* lds, LAS unsigned char* lds_epi, const Prob g, const Sched& S, const Epi& E, int wid) {
;     ...
;             PG8_LDB(B0, 0, 0); PG8_LDB(B1, 0, 1); PG8_SCHED; PG8_LDA(At, 0, 0); PG8_STAGE(PG8_SA(1, 1), a1, cA10, cA11);
;             PG8_WAIT_V(8); PG8_WAIT_L(0); PG8_BAR; PG8_MMA(0, 0, At, B0); PG8_MMA(0, 1, At, B1); PG8_BAR; PG8_SCHED;
;             PG8_LDA(At, 0, 1); PG8_STAGE(PG8_SB(0, 0), b2, vB0, vB1); PG8_STAGE(PG8_SB(0, 1), b2 + hstepB, vB0, vB1); PG8_STAGE(PG8_SA(0, 0), a2, cA00, cA01);
;             PG8_WAIT_V(8); PG8_WAIT_L(0); PG8_BAR; PG8_MMA(1, 0, At, B0); PG8_MMA(1, 1, At, B1); PG8_BAR; PG8_SCHED;
.LBB0_1248:
	ds_read_b128 v[24:27], v194
	ds_read_b128 v[28:31], v194 offset:1024
	ds_read_b128 v[16:19], v194 offset:2048
	ds_read_b128 v[20:23], v194 offset:3072
	ds_read_b128 v[8:11], v195
	ds_read_b128 v[12:15], v195 offset:1024
	ds_read_b128 v[0:3], v195 offset:2048
	ds_read_b128 v[4:7], v195 offset:3072
	s_add_u32 s30, s10, 0x80
	s_addc_u32 s31, s11, 0
	s_cmp_eq_u32 s59, 12
	s_cselect_b32 s35, s3, s31
	s_cselect_b32 s34, s54, s30
	s_cselect_b32 s31, s21, s58
	s_cselect_b32 s30, s55, s56
	v_lshl_add_u64 v[224:225], s[10:11], 0, v[178:179]
	s_add_i32 m0, s29, 0xc000
	ds_read_b128 v[182:185], v196
	ds_read_b128 v[186:189], v196 offset:1024
	ds_read_b128 v[200:203], v196 offset:2048
	ds_read_b128 v[204:207], v196 offset:3072
	ds_read_b128 v[208:211], v196 offset:4096
	ds_read_b128 v[212:215], v196 offset:5120
	ds_read_b128 v[216:219], v196 offset:6144
	ds_read_b128 v[220:223], v196 offset:7168
	global_load_lds_dwordx4 v[224:225], off
	v_lshl_add_u64 v[224:225], s[10:11], 0, v[176:177]
	s_add_i32 m0, s29, 0xe000
	s_nop 0
	global_load_lds_dwordx4 v[224:225], off
	s_waitcnt vmcnt(8)
	s_waitcnt lgkmcnt(0)
	s_barrier
	s_setprio 1
	s_waitcnt lgkmcnt(0)
	v_mfma_f32_16x16x128_f8f6f4 v[156:159], v[24:31], v[182:189], v[156:159]
	v_mfma_f32_16x16x128_f8f6f4 v[144:147], v[16:23], v[182:189], v[144:147]
	v_mfma_f32_16x16x128_f8f6f4 v[140:143], v[24:31], v[200:207], v[140:143]
	v_mfma_f32_16x16x128_f8f6f4 v[132:135], v[16:23], v[200:207], v[132:135]
	v_mfma_f32_16x16x128_f8f6f4 v[124:127], v[24:31], v[208:215], v[124:127]
	v_mfma_f32_16x16x128_f8f6f4 v[116:119], v[16:23], v[208:215], v[116:119]
	v_mfma_f32_16x16x128_f8f6f4 v[108:111], v[24:31], v[216:223], v[108:111]
	v_mfma_f32_16x16x128_f8f6f4 v[100:103], v[16:23], v[216:223], v[100:103]
	s_setprio 0
	s_setprio 1
	v_mfma_f32_16x16x128_f8f6f4 v[152:155], v[8:15], v[182:189], v[152:155]
	v_mfma_f32_16x16x128_f8f6f4 v[148:151], v[0:7], v[182:189], v[148:151]
	v_mfma_f32_16x16x128_f8f6f4 v[136:139], v[8:15], v[200:207], v[136:139]
	v_mfma_f32_16x16x128_f8f6f4 v[128:131], v[0:7], v[200:207], v[128:131]
	v_mfma_f32_16x16x128_f8f6f4 v[120:123], v[8:15], v[208:215], v[120:123]
	v_mfma_f32_16x16x128_f8f6f4 v[112:115], v[0:7], v[208:215], v[112:115]
	v_mfma_f32_16x16x128_f8f6f4 v[104:107], v[8:15], v[216:223], v[104:107]
	v_mfma_f32_16x16x128_f8f6f4 v[96:99], v[0:7], v[216:223], v[96:99]
	s_setprio 0
	s_barrier
	s_add_i32 s60, s50, s97
	v_lshl_add_u64 v[182:183], s[30:31], 0, v[162:163]
	s_mov_b32 m0, s60
	ds_read_b128 v[200:203], v196 offset:16384
	ds_read_b128 v[204:207], v196 offset:17408
	ds_read_b128 v[208:211], v196 offset:18432
	ds_read_b128 v[212:215], v196 offset:19456
	ds_read_b128 v[216:219], v196 offset:20480
	ds_read_b128 v[220:223], v196 offset:21504
	ds_read_b128 v[224:227], v196 offset:22528
	ds_read_b128 v[228:231], v196 offset:23552
	global_load_lds_dwordx4 v[182:183], off
	s_add_i32 m0, s60, 0x2000
	s_add_u32 s60, s30, 0x40000
	v_lshl_add_u64 v[184:185], s[30:31], 0, v[160:161]
	s_addc_u32 s61, s31, 0
	s_add_i32 s62, s51, s97
	global_load_lds_dwordx4 v[184:185], off
	v_lshl_add_u64 v[186:187], s[60:61], 0, v[162:163]
	s_mov_b32 m0, s62
	v_lshl_add_u64 v[188:189], s[34:35], 0, v[168:169]
	global_load_lds_dwordx4 v[186:187], off
	v_lshl_add_u64 v[186:187], s[60:61], 0, v[160:161]
	s_add_i32 m0, s62, 0x2000
	s_nop 0
	global_load_lds_dwordx4 v[186:187], off
	v_lshl_add_u64 v[186:187], s[34:35], 0, v[164:165]
	s_mov_b32 m0, s29
	s_nop 0
	global_load_lds_dwordx4 v[186:187], off
	s_mov_b32 m0, s43
	s_nop 0
	global_load_lds_dwordx4 v[188:189], off
	s_waitcnt vmcnt(8)
	s_waitcnt lgkmcnt(0)
	s_barrier
	s_setprio 1
	s_waitcnt lgkmcnt(0)
	v_mfma_f32_16x16x128_f8f6f4 v[92:95], v[24:31], v[200:207], v[92:95]
	v_mfma_f32_16x16x128_f8f6f4 v[84:87], v[16:23], v[200:207], v[84:87]
	v_mfma_f32_16x16x128_f8f6f4 v[76:79], v[24:31], v[208:215], v[76:79]
	v_mfma_f32_16x16x128_f8f6f4 v[68:71], v[16:23], v[208:215], v[68:71]
	v_mfma_f32_16x16x128_f8f6f4 v[60:63], v[24:31], v[216:223], v[60:63]
	v_mfma_f32_16x16x128_f8f6f4 v[52:55], v[16:23], v[216:223], v[52:55]
	v_mfma_f32_16x16x128_f8f6f4 v[44:47], v[24:31], v[224:231], v[44:47]
	v_mfma_f32_16x16x128_f8f6f4 v[36:39], v[16:23], v[224:231], v[36:39]
	s_setprio 0
	s_setprio 1
	v_mfma_f32_16x16x128_f8f6f4 v[88:91], v[8:15], v[200:207], v[88:91]
	v_mfma_f32_16x16x128_f8f6f4 v[80:83], v[0:7], v[200:207], v[80:83]
	v_mfma_f32_16x16x128_f8f6f4 v[72:75], v[8:15], v[208:215], v[72:75]
	v_mfma_f32_16x16x128_f8f6f4 v[64:67], v[0:7], v[208:215], v[64:67]
	v_mfma_f32_16x16x128_f8f6f4 v[56:59], v[8:15], v[216:223], v[56:59]
	v_mfma_f32_16x16x128_f8f6f4 v[48:51], v[0:7], v[216:223], v[48:51]
	v_mfma_f32_16x16x128_f8f6f4 v[40:43], v[8:15], v[224:231], v[40:43]
	v_mfma_f32_16x16x128_f8f6f4 v[32:35], v[0:7], v[224:231], v[32:35]
	s_setprio 0
	s_barrier
; #define PG8_STAGE(bufoff, gbase, o0, o1) do { \
;         __builtin_amdgcn_global_load_lds((const unsigned*)((const char*)(gbase) + (o0)), (LAS unsigned*)(lds + (bufoff) + ldsw), 16, 0, 0); \
;         __builtin_amdgcn_global_load_lds((const unsigned*)((const char*)(gbase) + (o1)), (LAS unsigned*)(lds + (bufoff) + ldsw + 8192), 16, 0, 0); } while (0)
; #define PG8_LDA(dst, b, h) do { _Pragma("unroll") for (int m = 0; m < 4; ++m) _Pragma("unroll") for (int k = 0; k < 2; ++k) dst[m][k] = *(const LAS bf16x8*)(lds + PG8_SA(b, h) + aoff + m * 2048 + k * 1024); } while (0)
; #define PG8_LDB(dst, b, h) do { _Pragma("unroll") for (int n = 0; n < 2; ++n) _Pragma("unroll") for (int k = 0; k < 2; ++k) dst[n][k] = *(const LAS bf16x8*)(lds + PG8_SB(b, h) + boff + n * 2048 + k * 1024); } while (0)
; #define PG8_WAIT_V(n) asm volatile("s_waitcnt vmcnt(" #n ")" ::: "memory")
; #define PG8_WAIT_L(n) asm volatile("s_waitcnt lgkmcnt(" #n ")" ::: "memory")
; #define PG8_BAR __builtin_amdgcn_s_barrier()
; #define PG8_SCHED __builtin_amdgcn_sched_barrier(0)
; template <class Epi, class Sched, class Prob>
; __device__ __forceinline__ void gemm_phase(LAS unsigned char* lds, LAS unsigned char* lds_epi, const Prob g, const Sched& S, const Epi& E, int wid) {
;     ...
;             PG8_LDB(B0, 1, 0); PG8_LDB(B1, 1, 1); PG8_SCHED; PG8_LDA(At, 1, 0); PG8_STAGE(PG8_SA(0, 1), a2, cA10, cA11);
;             PG8_WAIT_V(8); PG8_WAIT_L(0); PG8_BAR; PG8_MMA(0, 0, At, B0); PG8_MMA(0, 1, At, B1); PG8_BAR; PG8_SCHED;
;             PG8_LDA(At, 1, 1); PG8_STAGE(PG8_SB(1, 0), b3, vB0, vB1); PG8_STAGE(PG8_SB(1, 1), b3 + hstepB, vB0, vB1); PG8_STAGE(PG8_SA(1, 0), a3, cA00, cA01);
;             PG8_WAIT_V(8); PG8_WAIT_L(0); PG8_BAR; PG8_MMA(1, 0, At, B0); PG8_MMA(1, 1, At, B1); PG8_BAR; PG8_SCHED;
;         }
;         if constexpr (Prob::FP8) asm volatile("s_nop 7\n\ts_nop 7\n\ts_nop 7" ::: "memory");
;         if (wr == 0) PG8_BAR;
	s_add_i32 s60, 0, 0x18000
	s_add_i32 s61, 0, 0x1c000
	v_add_u32_e32 v12, s60, v191
	v_add_u32_e32 v28, s61, v191
	ds_read_b128 v[0:3], v12
	ds_read_b128 v[4:7], v12 offset:1024
	ds_read_b128 v[8:11], v12 offset:2048
	ds_read_b128 v[12:15], v12 offset:3072
	ds_read_b128 v[16:19], v28
	ds_read_b128 v[20:23], v28 offset:1024
	ds_read_b128 v[24:27], v28 offset:2048
	ds_read_b128 v[28:31], v28 offset:3072
	s_mov_b32 m0, s44
	v_lshl_add_u64 v[232:233], s[34:35], 0, v[166:167]
	ds_read_b128 v[200:203], v196 offset:32768
	ds_read_b128 v[204:207], v196 offset:33792
	ds_read_b128 v[208:211], v196 offset:34816
	ds_read_b128 v[212:215], v196 offset:35840
	ds_read_b128 v[216:219], v196 offset:36864
	ds_read_b128 v[220:223], v196 offset:37888
	ds_read_b128 v[224:227], v196 offset:38912
	ds_read_b128 v[228:231], v196 offset:39936
	global_load_lds_dwordx4 v[232:233], off
	v_lshl_add_u64 v[232:233], s[34:35], 0, v[170:171]
	s_mov_b32 m0, s45
	s_nop 0
	global_load_lds_dwordx4 v[232:233], off
	s_waitcnt vmcnt(8)
	s_waitcnt lgkmcnt(0)
	s_barrier
	s_setprio 1
	s_waitcnt lgkmcnt(0)
	v_mfma_f32_16x16x128_f8f6f4 v[156:159], v[0:7], v[200:207], v[156:159]
	v_mfma_f32_16x16x128_f8f6f4 v[144:147], v[8:15], v[200:207], v[144:147]
	v_mfma_f32_16x16x128_f8f6f4 v[140:143], v[0:7], v[208:215], v[140:143]
	v_mfma_f32_16x16x128_f8f6f4 v[132:135], v[8:15], v[208:215], v[132:135]
	v_mfma_f32_16x16x128_f8f6f4 v[124:127], v[0:7], v[216:223], v[124:127]
	v_mfma_f32_16x16x128_f8f6f4 v[116:119], v[8:15], v[216:223], v[116:119]
	v_mfma_f32_16x16x128_f8f6f4 v[108:111], v[0:7], v[224:231], v[108:111]
	v_mfma_f32_16x16x128_f8f6f4 v[100:103], v[8:15], v[224:231], v[100:103]
	s_setprio 0
	s_setprio 1
	v_mfma_f32_16x16x128_f8f6f4 v[152:155], v[16:23], v[200:207], v[152:155]
	v_mfma_f32_16x16x128_f8f6f4 v[148:151], v[24:31], v[200:207], v[148:151]
	v_mfma_f32_16x16x128_f8f6f4 v[136:139], v[16:23], v[208:215], v[136:139]
	v_mfma_f32_16x16x128_f8f6f4 v[128:131], v[24:31], v[208:215], v[128:131]
	v_mfma_f32_16x16x128_f8f6f4 v[120:123], v[16:23], v[216:223], v[120:123]
	v_mfma_f32_16x16x128_f8f6f4 v[112:115], v[24:31], v[216:223], v[112:115]
	v_mfma_f32_16x16x128_f8f6f4 v[104:107], v[16:23], v[224:231], v[104:107]
	v_mfma_f32_16x16x128_f8f6f4 v[96:99], v[24:31], v[224:231], v[96:99]
	s_setprio 0
	s_barrier
	s_add_i32 s34, s60, s97
	v_lshl_add_u64 v[182:183], v[182:183], 0, s[14:15]
	s_mov_b32 m0, s34
	ds_read_b128 v[200:203], v196 offset:49152
	ds_read_b128 v[204:207], v196 offset:50176
	ds_read_b128 v[208:211], v196 offset:51200
	ds_read_b128 v[212:215], v196 offset:52224
	ds_read_b128 v[216:219], v196 offset:53248
	ds_read_b128 v[220:223], v196 offset:54272
	ds_read_b128 v[224:227], v196 offset:55296
	ds_read_b128 v[228:231], v196 offset:56320
	global_load_lds_dwordx4 v[182:183], off
	s_add_i32 m0, s34, 0x2000
	s_add_u32 s30, s30, 0x40080
	v_lshl_add_u64 v[182:183], v[184:185], 0, s[14:15]
	s_addc_u32 s31, s31, 0
	s_add_i32 s34, s61, s97
	global_load_lds_dwordx4 v[182:183], off
	v_lshl_add_u64 v[182:183], s[30:31], 0, v[162:163]
	s_mov_b32 m0, s34
	s_nop 0
	global_load_lds_dwordx4 v[182:183], off
	v_lshl_add_u64 v[182:183], s[30:31], 0, v[160:161]
	s_add_i32 m0, s34, 0x2000
	s_nop 0
	global_load_lds_dwordx4 v[182:183], off
	v_lshl_add_u64 v[182:183], v[186:187], 0, s[14:15]
	s_mov_b32 m0, s48
	s_nop 0
	global_load_lds_dwordx4 v[182:183], off
	v_lshl_add_u64 v[182:183], v[188:189], 0, s[14:15]
	s_mov_b32 m0, s49
	s_nop 0
	global_load_lds_dwordx4 v[182:183], off
	s_waitcnt vmcnt(8)
	s_waitcnt lgkmcnt(0)
	s_barrier
	s_setprio 1
	s_waitcnt lgkmcnt(0)
	v_mfma_f32_16x16x128_f8f6f4 v[92:95], v[0:7], v[200:207], v[92:95]
	v_mfma_f32_16x16x128_f8f6f4 v[84:87], v[8:15], v[200:207], v[84:87]
	v_mfma_f32_16x16x128_f8f6f4 v[76:79], v[0:7], v[208:215], v[76:79]
	v_mfma_f32_16x16x128_f8f6f4 v[68:71], v[8:15], v[208:215], v[68:71]
	v_mfma_f32_16x16x128_f8f6f4 v[60:63], v[0:7], v[216:223], v[60:63]
	v_mfma_f32_16x16x128_f8f6f4 v[52:55], v[8:15], v[216:223], v[52:55]
	v_mfma_f32_16x16x128_f8f6f4 v[44:47], v[0:7], v[224:231], v[44:47]
	v_mfma_f32_16x16x128_f8f6f4 v[36:39], v[8:15], v[224:231], v[36:39]
	s_setprio 0
	s_setprio 1
	v_mfma_f32_16x16x128_f8f6f4 v[88:91], v[16:23], v[200:207], v[88:91]
	v_mfma_f32_16x16x128_f8f6f4 v[80:83], v[24:31], v[200:207], v[80:83]
	v_mfma_f32_16x16x128_f8f6f4 v[72:75], v[16:23], v[208:215], v[72:75]
	v_mfma_f32_16x16x128_f8f6f4 v[64:67], v[24:31], v[208:215], v[64:67]
	v_mfma_f32_16x16x128_f8f6f4 v[56:59], v[16:23], v[216:223], v[56:59]
	v_mfma_f32_16x16x128_f8f6f4 v[48:51], v[24:31], v[216:223], v[48:51]
	v_mfma_f32_16x16x128_f8f6f4 v[40:43], v[16:23], v[224:231], v[40:43]
	v_mfma_f32_16x16x128_f8f6f4 v[32:35], v[24:31], v[224:231], v[32:35]
	s_setprio 0
	s_barrier
	s_add_i32 s59, s59, 2
	s_add_u32 s10, s10, 0x100
	s_addc_u32 s11, s11, 0
	s_add_u32 s56, s56, 0x100
	s_addc_u32 s58, s58, 0
	s_cmp_gt_u32 s59, 13
	s_cbranch_scc0 .LBB0_1248
	v_readlane_b32 s10, v254, 27
	v_readlane_b32 s11, v254, 28
	s_and_b64 vcc, exec, s[10:11]
	s_cbranch_vccz .LBB0_1251
	s_barrier

; #define PG8_STAGE(bufoff, gbase, o0, o1) do { \
;         __builtin_amdgcn_global_load_lds((const unsigned*)((const char*)(gbase) + (o0)), (LAS unsigned*)(lds + (bufoff) + ldsw), 16, 0, 0); \
;         __builtin_amdgcn_global_load_lds((const unsigned*)((const char*)(gbase) + (o1)), (LAS unsigned*)(lds + (bufoff) + ldsw + 8192), 16, 0, 0); } while (0)
; #define PG8_LDA(dst, b, h) do { _Pragma("unroll") for (int m = 0; m < 4; ++m) _Pragma("unroll") for (int k = 0; k < 2; ++k) dst[m][k] = *(const LAS bf16x8*)(lds + PG8_SA(b, h) + aoff + m * 2048 + k * 1024); } while (0)
; #define PG8_LDB(dst, b, h) do { _Pragma("unroll") for (int n = 0; n < 2; ++n) _Pragma("unroll") for (int k = 0; k < 2; ++k) dst[n][k] = *(const LAS bf16x8*)(lds + PG8_SB(b, h) + boff + n * 2048 + k * 1024); } while (0)
; #define PG8_WAIT_V(n) asm volatile("s_waitcnt vmcnt(" #n ")" ::: "memory")
; #define PG8_WAIT_L(n) asm volatile("s_waitcnt lgkmcnt(" #n ")" ::: "memory")
; #define PG8_BAR __builtin_amdgcn_s_barrier()
; #define PG8_SCHED __builtin_amdgcn_sched_barrier(0)
; template <class Epi, class Sched, class Prob>
; __device__ __forceinline__ void gemm_phase(LAS unsigned char* lds, LAS unsigned char* lds_epi, const Prob g, const Sched& S, const Epi& E, int wid) {
;     ...
;             PG8_LDB(B0, 0, 0); PG8_LDB(B1, 0, 1); PG8_SCHED; PG8_LDA(At, 0, 0); PG8_STAGE(PG8_SA(1, 1), a1, cA10, cA11);
;             PG8_WAIT_V(8); PG8_WAIT_L(0); PG8_BAR; PG8_MMA(0, 0, At, B0); PG8_MMA(0, 1, At, B1); PG8_BAR; PG8_SCHED;
;             PG8_LDA(At, 0, 1); PG8_STAGE(PG8_SB(0, 0), b2, vB0, vB1); PG8_STAGE(PG8_SB(0, 1), b2 + hstepB, vB0, vB1); PG8_STAGE(PG8_SA(0, 0), a2, cA00, cA01);
;             PG8_WAIT_V(8); PG8_WAIT_L(0); PG8_BAR; PG8_MMA(1, 0, At, B0); PG8_MMA(1, 1, At, B1); PG8_BAR; PG8_SCHED;
.LBB0_2091:
	ds_read_b128 v[24:27], v199
	ds_read_b128 v[28:31], v199 offset:1024
	ds_read_b128 v[16:19], v199 offset:2048
	ds_read_b128 v[20:23], v199 offset:3072
	ds_read_b128 v[8:11], v200
	ds_read_b128 v[12:15], v200 offset:1024
	ds_read_b128 v[0:3], v200 offset:2048
	ds_read_b128 v[4:7], v200 offset:3072
	s_add_u32 s40, s36, 0x80
	s_addc_u32 s41, s37, 0
	s_cmp_eq_u32 s69, 12
	s_cselect_b64 vcc, -1, 0
	s_cselect_b32 s41, s11, s41
	s_cselect_b32 s40, s29, s40
	v_cndmask_b32_e32 v185, v183, v181, vcc
	v_cndmask_b32_e32 v184, v182, v180, vcc
	v_lshl_add_u64 v[228:229], s[36:37], 0, v[176:177]
	s_add_i32 m0, s35, 0xc000
	ds_read_b128 v[186:189], v201
	ds_read_b128 v[190:193], v201 offset:1024
	ds_read_b128 v[204:207], v201 offset:2048
	ds_read_b128 v[208:211], v201 offset:3072
	ds_read_b128 v[212:215], v201 offset:4096
	ds_read_b128 v[216:219], v201 offset:5120
	ds_read_b128 v[220:223], v201 offset:6144
	ds_read_b128 v[224:227], v201 offset:7168
	global_load_lds_dwordx4 v[228:229], off
	v_lshl_add_u64 v[228:229], s[36:37], 0, v[174:175]
	s_add_i32 m0, s35, 0xe000
	s_nop 0
	global_load_lds_dwordx4 v[228:229], off
	s_waitcnt vmcnt(8)
	s_waitcnt lgkmcnt(0)
	s_barrier
	s_setprio 1
	s_waitcnt lgkmcnt(0)
	v_mfma_f32_16x16x128_f8f6f4 v[156:159], v[24:31], v[186:193], v[156:159]
	v_mfma_f32_16x16x128_f8f6f4 v[152:155], v[16:23], v[186:193], v[152:155]
	v_mfma_f32_16x16x128_f8f6f4 v[140:143], v[24:31], v[204:211], v[140:143]
	v_mfma_f32_16x16x128_f8f6f4 v[136:139], v[16:23], v[204:211], v[136:139]
	v_mfma_f32_16x16x128_f8f6f4 v[124:127], v[24:31], v[212:219], v[124:127]
	v_mfma_f32_16x16x128_f8f6f4 v[120:123], v[16:23], v[212:219], v[120:123]
	v_mfma_f32_16x16x128_f8f6f4 v[108:111], v[24:31], v[220:227], v[108:111]
	v_mfma_f32_16x16x128_f8f6f4 v[104:107], v[16:23], v[220:227], v[104:107]
	s_setprio 0
	s_setprio 1
	v_mfma_f32_16x16x128_f8f6f4 v[148:151], v[8:15], v[186:193], v[148:151]
	v_mfma_f32_16x16x128_f8f6f4 v[144:147], v[0:7], v[186:193], v[144:147]
	v_mfma_f32_16x16x128_f8f6f4 v[132:135], v[8:15], v[204:211], v[132:135]
	v_mfma_f32_16x16x128_f8f6f4 v[128:131], v[0:7], v[204:211], v[128:131]
	v_mfma_f32_16x16x128_f8f6f4 v[116:119], v[8:15], v[212:219], v[116:119]
	v_mfma_f32_16x16x128_f8f6f4 v[112:115], v[0:7], v[212:219], v[112:115]
	v_mfma_f32_16x16x128_f8f6f4 v[100:103], v[8:15], v[220:227], v[100:103]
	v_mfma_f32_16x16x128_f8f6f4 v[96:99], v[0:7], v[220:227], v[96:99]
	s_setprio 0
	s_barrier
	s_add_i32 s70, s63, s97
	v_lshl_add_u64 v[186:187], v[184:185], 0, v[160:161]
	s_mov_b32 m0, s70
	ds_read_b128 v[204:207], v201 offset:16384
	ds_read_b128 v[208:211], v201 offset:17408
	ds_read_b128 v[212:215], v201 offset:18432
	ds_read_b128 v[216:219], v201 offset:19456
	ds_read_b128 v[220:223], v201 offset:20480
	ds_read_b128 v[224:227], v201 offset:21504
	ds_read_b128 v[228:231], v201 offset:22528
	ds_read_b128 v[232:235], v201 offset:23552
	global_load_lds_dwordx4 v[186:187], off
	v_lshl_add_u64 v[188:189], v[184:185], 0, v[162:163]
	s_add_i32 m0, s70, 0x2000
	v_lshl_add_u64 v[190:191], v[184:185], 0, s[12:13]
	s_add_i32 s70, s64, s97
	global_load_lds_dwordx4 v[188:189], off
	v_lshl_add_u64 v[192:193], v[190:191], 0, v[160:161]
	s_mov_b32 m0, s70
	v_lshl_add_u64 v[190:191], v[190:191], 0, v[162:163]
	global_load_lds_dwordx4 v[192:193], off
	s_add_i32 m0, s70, 0x2000
	v_lshl_add_u64 v[192:193], s[40:41], 0, v[168:169]
	global_load_lds_dwordx4 v[190:191], off
	v_lshl_add_u64 v[190:191], s[40:41], 0, v[164:165]
	s_mov_b32 m0, s35
	s_nop 0
	global_load_lds_dwordx4 v[190:191], off
	s_mov_b32 m0, s58
	s_nop 0
	global_load_lds_dwordx4 v[192:193], off
	s_waitcnt vmcnt(8)
	s_waitcnt lgkmcnt(0)
	s_barrier
	s_setprio 1
	s_waitcnt lgkmcnt(0)
	v_mfma_f32_16x16x128_f8f6f4 v[92:95], v[24:31], v[204:211], v[92:95]
	v_mfma_f32_16x16x128_f8f6f4 v[88:91], v[16:23], v[204:211], v[88:91]
	v_mfma_f32_16x16x128_f8f6f4 v[76:79], v[24:31], v[212:219], v[76:79]
	v_mfma_f32_16x16x128_f8f6f4 v[72:75], v[16:23], v[212:219], v[72:75]
	v_mfma_f32_16x16x128_f8f6f4 v[60:63], v[24:31], v[220:227], v[60:63]
	v_mfma_f32_16x16x128_f8f6f4 v[56:59], v[16:23], v[220:227], v[56:59]
	v_mfma_f32_16x16x128_f8f6f4 v[44:47], v[24:31], v[228:235], v[44:47]
	v_mfma_f32_16x16x128_f8f6f4 v[40:43], v[16:23], v[228:235], v[40:43]
	s_setprio 0
	s_setprio 1
	v_mfma_f32_16x16x128_f8f6f4 v[84:87], v[8:15], v[204:211], v[84:87]
	v_mfma_f32_16x16x128_f8f6f4 v[80:83], v[0:7], v[204:211], v[80:83]
	v_mfma_f32_16x16x128_f8f6f4 v[68:71], v[8:15], v[212:219], v[68:71]
	v_mfma_f32_16x16x128_f8f6f4 v[64:67], v[0:7], v[212:219], v[64:67]
	v_mfma_f32_16x16x128_f8f6f4 v[52:55], v[8:15], v[220:227], v[52:55]
	v_mfma_f32_16x16x128_f8f6f4 v[48:51], v[0:7], v[220:227], v[48:51]
	v_mfma_f32_16x16x128_f8f6f4 v[36:39], v[8:15], v[228:235], v[36:39]
	v_mfma_f32_16x16x128_f8f6f4 v[32:35], v[0:7], v[228:235], v[32:35]
	s_setprio 0
	s_barrier
; #define PG8_STAGE(bufoff, gbase, o0, o1) do { \
;         __builtin_amdgcn_global_load_lds((const unsigned*)((const char*)(gbase) + (o0)), (LAS unsigned*)(lds + (bufoff) + ldsw), 16, 0, 0); \
;         __builtin_amdgcn_global_load_lds((const unsigned*)((const char*)(gbase) + (o1)), (LAS unsigned*)(lds + (bufoff) + ldsw + 8192), 16, 0, 0); } while (0)
; #define PG8_LDA(dst, b, h) do { _Pragma("unroll") for (int m = 0; m < 4; ++m) _Pragma("unroll") for (int k = 0; k < 2; ++k) dst[m][k] = *(const LAS bf16x8*)(lds + PG8_SA(b, h) + aoff + m * 2048 + k * 1024); } while (0)
; #define PG8_LDB(dst, b, h) do { _Pragma("unroll") for (int n = 0; n < 2; ++n) _Pragma("unroll") for (int k = 0; k < 2; ++k) dst[n][k] = *(const LAS bf16x8*)(lds + PG8_SB(b, h) + boff + n * 2048 + k * 1024); } while (0)
; #define PG8_WAIT_V(n) asm volatile("s_waitcnt vmcnt(" #n ")" ::: "memory")
; #define PG8_WAIT_L(n) asm volatile("s_waitcnt lgkmcnt(" #n ")" ::: "memory")
; #define PG8_BAR __builtin_amdgcn_s_barrier()
; #define PG8_SCHED __builtin_amdgcn_sched_barrier(0)
; template <class Epi, class Sched, class Prob>
; __device__ __forceinline__ void gemm_phase(LAS unsigned char* lds, LAS unsigned char* lds_epi, const Prob g, const Sched& S, const Epi& E, int wid) {
;     ...
;             PG8_LDB(B0, 1, 0); PG8_LDB(B1, 1, 1); PG8_SCHED; PG8_LDA(At, 1, 0); PG8_STAGE(PG8_SA(0, 1), a2, cA10, cA11);
;             PG8_WAIT_V(8); PG8_WAIT_L(0); PG8_BAR; PG8_MMA(0, 0, At, B0); PG8_MMA(0, 1, At, B1); PG8_BAR; PG8_SCHED;
;             PG8_LDA(At, 1, 1); PG8_STAGE(PG8_SB(1, 0), b3, vB0, vB1); PG8_STAGE(PG8_SB(1, 1), b3 + hstepB, vB0, vB1); PG8_STAGE(PG8_SA(1, 0), a3, cA00, cA01);
;             PG8_WAIT_V(8); PG8_WAIT_L(0); PG8_BAR; PG8_MMA(1, 0, At, B0); PG8_MMA(1, 1, At, B1); PG8_BAR; PG8_SCHED;
;         }
;         if constexpr (Prob::FP8) asm volatile("s_nop 7\n\ts_nop 7\n\ts_nop 7" ::: "memory");
;         if (wr == 0) PG8_BAR;
	s_add_i32 s70, 0, 0x18000
	s_add_i32 s71, 0, 0x1c000
	v_add_u32_e32 v12, s70, v195
	v_add_u32_e32 v28, s71, v195
	ds_read_b128 v[0:3], v12
	ds_read_b128 v[4:7], v12 offset:1024
	ds_read_b128 v[8:11], v12 offset:2048
	ds_read_b128 v[12:15], v12 offset:3072
	ds_read_b128 v[16:19], v28
	ds_read_b128 v[20:23], v28 offset:1024
	ds_read_b128 v[24:27], v28 offset:2048
	ds_read_b128 v[28:31], v28 offset:3072
	s_mov_b32 m0, s59
	v_lshl_add_u64 v[236:237], s[40:41], 0, v[166:167]
	ds_read_b128 v[204:207], v201 offset:32768
	ds_read_b128 v[208:211], v201 offset:33792
	ds_read_b128 v[212:215], v201 offset:34816
	ds_read_b128 v[216:219], v201 offset:35840
	ds_read_b128 v[220:223], v201 offset:36864
	ds_read_b128 v[224:227], v201 offset:37888
	ds_read_b128 v[228:231], v201 offset:38912
	ds_read_b128 v[232:235], v201 offset:39936
	global_load_lds_dwordx4 v[236:237], off
	v_lshl_add_u64 v[236:237], s[40:41], 0, v[170:171]
	s_mov_b32 m0, s60
	s_nop 0
	global_load_lds_dwordx4 v[236:237], off
	s_waitcnt vmcnt(8)
	s_waitcnt lgkmcnt(0)
	s_barrier
	s_setprio 1
	s_waitcnt lgkmcnt(0)
	v_mfma_f32_16x16x128_f8f6f4 v[156:159], v[0:7], v[204:211], v[156:159]
	v_mfma_f32_16x16x128_f8f6f4 v[152:155], v[8:15], v[204:211], v[152:155]
	v_mfma_f32_16x16x128_f8f6f4 v[140:143], v[0:7], v[212:219], v[140:143]
	v_mfma_f32_16x16x128_f8f6f4 v[136:139], v[8:15], v[212:219], v[136:139]
	v_mfma_f32_16x16x128_f8f6f4 v[124:127], v[0:7], v[220:227], v[124:127]
	v_mfma_f32_16x16x128_f8f6f4 v[120:123], v[8:15], v[220:227], v[120:123]
	v_mfma_f32_16x16x128_f8f6f4 v[108:111], v[0:7], v[228:235], v[108:111]
	v_mfma_f32_16x16x128_f8f6f4 v[104:107], v[8:15], v[228:235], v[104:107]
	s_setprio 0
	s_setprio 1
	v_mfma_f32_16x16x128_f8f6f4 v[148:151], v[16:23], v[204:211], v[148:151]
	v_mfma_f32_16x16x128_f8f6f4 v[144:147], v[24:31], v[204:211], v[144:147]
	v_mfma_f32_16x16x128_f8f6f4 v[132:135], v[16:23], v[212:219], v[132:135]
	v_mfma_f32_16x16x128_f8f6f4 v[128:131], v[24:31], v[212:219], v[128:131]
	v_mfma_f32_16x16x128_f8f6f4 v[116:119], v[16:23], v[220:227], v[116:119]
	v_mfma_f32_16x16x128_f8f6f4 v[112:115], v[24:31], v[220:227], v[112:115]
	v_mfma_f32_16x16x128_f8f6f4 v[100:103], v[16:23], v[228:235], v[100:103]
	v_mfma_f32_16x16x128_f8f6f4 v[96:99], v[24:31], v[228:235], v[96:99]
	s_setprio 0
	s_barrier
	s_add_i32 s40, s70, s97
	v_lshl_add_u64 v[186:187], v[186:187], 0, s[18:19]
	s_mov_b32 m0, s40
	ds_read_b128 v[204:207], v201 offset:49152
	ds_read_b128 v[208:211], v201 offset:50176
	ds_read_b128 v[212:215], v201 offset:51200
	ds_read_b128 v[216:219], v201 offset:52224
	ds_read_b128 v[220:223], v201 offset:53248
	ds_read_b128 v[224:227], v201 offset:54272
	ds_read_b128 v[228:231], v201 offset:55296
	ds_read_b128 v[232:235], v201 offset:56320
	global_load_lds_dwordx4 v[186:187], off
	v_lshl_add_u64 v[186:187], v[188:189], 0, s[18:19]
	s_add_i32 m0, s40, 0x2000
	v_lshl_add_u64 v[184:185], v[184:185], 0, s[20:21]
	s_add_i32 s40, s71, s97
	global_load_lds_dwordx4 v[186:187], off
	v_lshl_add_u64 v[186:187], v[184:185], 0, v[160:161]
	s_mov_b32 m0, s40
	v_lshl_add_u64 v[184:185], v[184:185], 0, v[162:163]
	global_load_lds_dwordx4 v[186:187], off
	s_add_i32 m0, s40, 0x2000
	s_nop 0
	global_load_lds_dwordx4 v[184:185], off
	v_lshl_add_u64 v[184:185], v[190:191], 0, s[18:19]
	s_mov_b32 m0, s61
	s_nop 0
	global_load_lds_dwordx4 v[184:185], off
	v_lshl_add_u64 v[184:185], v[192:193], 0, s[18:19]
	s_mov_b32 m0, s62
	s_nop 0
	global_load_lds_dwordx4 v[184:185], off
	s_waitcnt vmcnt(8)
	s_waitcnt lgkmcnt(0)
	s_barrier
	s_setprio 1
	s_waitcnt lgkmcnt(0)
	v_mfma_f32_16x16x128_f8f6f4 v[92:95], v[0:7], v[204:211], v[92:95]
	v_mfma_f32_16x16x128_f8f6f4 v[88:91], v[8:15], v[204:211], v[88:91]
	v_mfma_f32_16x16x128_f8f6f4 v[76:79], v[0:7], v[212:219], v[76:79]
	v_mfma_f32_16x16x128_f8f6f4 v[72:75], v[8:15], v[212:219], v[72:75]
	v_mfma_f32_16x16x128_f8f6f4 v[60:63], v[0:7], v[220:227], v[60:63]
	v_mfma_f32_16x16x128_f8f6f4 v[56:59], v[8:15], v[220:227], v[56:59]
	v_mfma_f32_16x16x128_f8f6f4 v[44:47], v[0:7], v[228:235], v[44:47]
	v_mfma_f32_16x16x128_f8f6f4 v[40:43], v[8:15], v[228:235], v[40:43]
	s_setprio 0
	s_setprio 1
	v_mfma_f32_16x16x128_f8f6f4 v[84:87], v[16:23], v[204:211], v[84:87]
	v_mfma_f32_16x16x128_f8f6f4 v[80:83], v[24:31], v[204:211], v[80:83]
	v_mfma_f32_16x16x128_f8f6f4 v[68:71], v[16:23], v[212:219], v[68:71]
	v_mfma_f32_16x16x128_f8f6f4 v[64:67], v[24:31], v[212:219], v[64:67]
	v_mfma_f32_16x16x128_f8f6f4 v[52:55], v[16:23], v[220:227], v[52:55]
	v_mfma_f32_16x16x128_f8f6f4 v[48:51], v[24:31], v[220:227], v[48:51]
	v_mfma_f32_16x16x128_f8f6f4 v[36:39], v[16:23], v[228:235], v[36:39]
	v_mfma_f32_16x16x128_f8f6f4 v[32:35], v[24:31], v[228:235], v[32:35]
	s_setprio 0
	s_barrier
	s_add_i32 s69, s69, 2
	s_add_u32 s36, s36, 0x100
	s_addc_u32 s37, s37, 0
	s_cmp_gt_u32 s69, 13
	v_lshl_add_u64 v[182:183], v[182:183], 0, s[22:23]
	s_cbranch_scc0 .LBB0_2091
	v_readlane_b32 s36, v254, 27
	v_readlane_b32 s37, v254, 28
	s_and_b64 vcc, exec, s[36:37]
	s_cbranch_vccz .LBB0_2094
	s_barrier
